# T5 start stagger reduced from 400 to 100 ticks per workgroup group (the prefetching epilogues tolerate the HBM bursts)
# speedup vs baseline: 1.0026x; 1.0026x over previous
; __global__ void __launch_bounds__(NT, 2) fwd_kernel(Params p) {
;     ...
;     { const unsigned long long t0 = __builtin_amdgcn_s_memrealtime(), w = (unsigned long long)((GB >> 3) & 7) * STAG_TICKS;
;       while (__builtin_amdgcn_s_memrealtime() - t0 < w) __builtin_amdgcn_s_sleep(4); }
.LBB0_2001:
	s_or_b64 exec, exec, s[2:3]
	s_memrealtime s[2:3]
	s_memrealtime s[0:1]
	s_bfe_u32 s4, s87, 0x30003
	s_mov_b32 s5, 0
	s_mulk_i32 s4, 0x64
	v_mov_b64_e32 v[0:1], s[4:5]
	s_waitcnt lgkmcnt(0)
	s_sub_u32 s0, s0, s2
	s_subb_u32 s1, s1, s3
	v_cmp_ge_u64_e32 vcc, s[0:1], v[0:1]
	v_readlane_b32 s38, v242, 13
	v_readlane_b32 s39, v242, 14
	s_cbranch_vccnz .LBB0_2004
	v_mov_b64_e32 v[0:1], s[4:5]
